# prologue weight transposes: thread index built from the rotated workgroup index (pieces of an output line written by one XCD)
# baseline (speedup 1.0000x reference)
;     const size_t total = (size_t)N * (K / 8);
; #pragma unroll 1
;     for (size_t i = (size_t)bid * NTHR + threadIdx.x; i < total; i += (size_t)nb * NTHR) {
;         const int n = (int)(i % N), kc = (int)(i / N);
;         float v[8];
; #pragma unroll
;         for (int j = 0; j < 8; ++j) v[j] = W[(size_t)(kc * 8 + j) * N + n];
;         uint4 r; r.x = pack2(v[0], v[1]); r.y = pack2(v[2], v[3]); r.z = pack2(v[4], v[5]); r.w = pack2(v[6], v[7]);
;         if (FRAG) *(uint4*)&WT[((size_t)((kc >> 1) * (N / 32) + (n >> 5)) * 64 + (n & 31) + 32 * (kc & 1)) * 8] = r;
;         else *(uint4*)&WT[(size_t)n * K + kc * 8] = r;
;     }
;     ...
;     transpose_cvt(P.in[10], 1024, 3072, (bfr*)(P.ws + WS_WINT0), bid, nb);
;     transpose_cvt(P.in[11], 1024, 1024, (bfr*)(P.ws + WS_WOUTT0), bid, nb);
;     transpose_cvt(P.in[22], 1024, 1280, (bfr*)(P.ws + WS_WINT1), bid, nb);
;     transpose_cvt(P.in[23], 1024, 1024, (bfr*)(P.ws + WS_WOUTT1), bid, nb);
;     transpose_cvt<1>(P.in[36], 1024, 256, (bfr*)(P.ws + WS_ROUT), bid, nb);
;     transpose_cvt<1>(P.in[36] + 1024 * 256, 1024, 256, (bfr*)(P.ws + WS_ROUT) + 256 * 1024, bid, nb);
;     transpose_cvt(P.in[34], 512, 512, (bfr*)(P.ws + WS_GLUT), bid, nb);
.LBB0_15:
	v_readlane_b32 s0, v253, 10
	s_cmpk_lg_u32 s0, 0x100
	s_cbranch_scc1 .Ltr_orig
	s_mov_b32 s1, 0
	s_mov_b32 s45, 0
	v_writelane_b32 v253, s1, 11
	v_and_b32_e32 v66, 0xff, v0
	v_and_b32_e32 v64, 31, v0
	s_and_b32 s96, s44, 7
	s_lshl_b32 s96, s96, 5
	s_lshr_b32 s97, s44, 3
	s_or_b32 s96, s96, s97
	v_lshl_or_b32 v2, s96, 9, v0
	v_readlane_b32 s4, v253, 39
	v_readlane_b32 s5, v253, 40
	v_readlane_b32 s6, v253, 41
	v_readlane_b32 s7, v253, 42
	v_readlane_b32 s8, v253, 63
	v_readlane_b32 s9, v252, 0
	v_readlane_b32 s10, v252, 1
	v_readlane_b32 s11, v252, 2
	v_readlane_b32 s12, v252, 11
	v_readlane_b32 s13, v252, 12
	v_readlane_b32 s16, v252, 7
	v_readlane_b32 s17, v252, 8
	s_mov_b32 s2, 0xaaaaaaab
	s_mov_b32 s3, 0xcccccccd
	s_mov_b32 s20, 0x18000
	s_mov_b32 s21, 0xa000
	v_mov_b32_e32 v23, v2
	v_mul_hi_u32 v24, v23, s2
	v_lshrrev_b32_e32 v24, 11, v24
	v_mul_u32_u24_e32 v25, 0xc00, v24
	v_sub_u32_e32 v25, v23, v25
	v_mul_lo_u32 v3, v24, s20
	v_lshl_add_u32 v3, v25, 2, v3
	v_lshlrev_b32_e32 v25, 11, v25
	v_lshl_add_u32 v12, v24, 4, v25
	v_add_u32_e32 v12, 0x28000, v12
	v_add_u32_e32 v23, 0x20000, v2
	v_mul_hi_u32 v24, v23, s2
	v_lshrrev_b32_e32 v24, 11, v24
	v_mul_u32_u24_e32 v25, 0xc00, v24
	v_sub_u32_e32 v25, v23, v25
	v_mul_lo_u32 v4, v24, s20
	v_lshl_add_u32 v4, v25, 2, v4
	v_lshlrev_b32_e32 v25, 11, v25
	v_lshl_add_u32 v13, v24, 4, v25
	v_add_u32_e32 v13, 0x28000, v13
	v_add_u32_e32 v23, 0x40000, v2
	v_mul_hi_u32 v24, v23, s2
	v_lshrrev_b32_e32 v24, 11, v24
	v_mul_u32_u24_e32 v25, 0xc00, v24
	v_sub_u32_e32 v25, v23, v25
	v_mul_lo_u32 v5, v24, s20
	v_lshl_add_u32 v5, v25, 2, v5
	v_lshlrev_b32_e32 v25, 11, v25
	v_lshl_add_u32 v14, v24, 4, v25
	v_add_u32_e32 v14, 0x28000, v14
	v_lshrrev_b32_e32 v24, 10, v2
	v_and_b32_e32 v25, 0x3ff, v2
	v_lshlrev_b32_e32 v6, 15, v24
	v_lshl_add_u32 v6, v25, 2, v6
	v_mov_b32_e32 v8, v6
	v_lshlrev_b32_e32 v25, 11, v25
	v_lshl_add_u32 v15, v24, 4, v25
	v_add_u32_e32 v17, 0xaa8000, v15
	v_add_u32_e32 v15, 0x628000, v15
	v_mov_b32_e32 v23, v2
	v_mul_hi_u32 v24, v23, s3
	v_lshrrev_b32_e32 v24, 10, v24
	v_mul_u32_u24_e32 v25, 0x500, v24
	v_sub_u32_e32 v25, v23, v25
	v_mul_lo_u32 v7, v24, s21
	v_lshl_add_u32 v7, v25, 2, v7
	v_lshlrev_b32_e32 v25, 11, v25
	v_lshl_add_u32 v16, v24, 4, v25
	v_add_u32_e32 v16, 0x828000, v16
	v_add_u32_e32 v23, 0x20000, v2
	v_mul_hi_u32 v24, v23, s3
	v_lshrrev_b32_e32 v24, 10, v24
	v_mul_u32_u24_e32 v25, 0x500, v24
	v_sub_u32_e32 v25, v23, v25
	v_mul_lo_u32 v9, v24, s21
	v_lshl_add_u32 v9, v25, 2, v9
	v_lshlrev_b32_e32 v25, 11, v25
	v_lshl_add_u32 v18, v24, 4, v25
	v_add_u32_e32 v18, 0x828000, v18
	v_lshrrev_b32_e32 v24, 8, v2
	v_lshlrev_b32_e32 v10, 13, v24
	v_lshl_add_u32 v10, v66, 2, v10
	v_lshrrev_b32_e32 v24, 6, v2
	v_and_b32_e32 v24, 0x1f8, v24
	v_bfe_u32 v25, v2, 5, 3
	v_or_b32_e32 v24, v24, v25
	v_lshrrev_b32_e32 v25, 3, v2
	v_and_b32_e32 v25, 32, v25
	v_lshlrev_b32_e32 v24, 6, v24
	v_or3_b32 v24, v24, v25, v64
	v_lshlrev_b32_e32 v24, 4, v24
	v_add_u32_e32 v19, 0xca8000, v24
	v_add_u32_e32 v20, 0xd28000, v24
	v_lshlrev_b32_e32 v11, 2, v0
	v_mov_b32_e32 v24, s96
	v_lshl_add_u32 v11, v24, 14, v11
	v_lshlrev_b32_e32 v21, 10, v0
	v_lshl_add_u32 v21, v24, 4, v21
	v_add_u32_e32 v21, 0xda8000, v21
	v_readlane_b32 s18, v253, 63
	v_readlane_b32 s19, v252, 0
	s_add_u32 s14, s12, 0x100000
	s_addc_u32 s15, s13, 0
	global_load_dword v70, v3, s[4:5]
	global_load_dword v78, v4, s[4:5]
	global_load_dword v86, v5, s[4:5]
	global_load_dword v94, v6, s[6:7]
	s_add_u32 s4, s4, 0x3000
	s_addc_u32 s5, s5, 0
	s_add_u32 s6, s6, 0x1000
	s_addc_u32 s7, s7, 0
	global_load_dword v71, v3, s[4:5]
	global_load_dword v79, v4, s[4:5]
	global_load_dword v87, v5, s[4:5]
	global_load_dword v95, v6, s[6:7]
	s_add_u32 s4, s4, 0x3000
	s_addc_u32 s5, s5, 0
	s_add_u32 s6, s6, 0x1000
	s_addc_u32 s7, s7, 0
	global_load_dword v72, v3, s[4:5]
	global_load_dword v80, v4, s[4:5]
	global_load_dword v88, v5, s[4:5]
	global_load_dword v96, v6, s[6:7]
	s_add_u32 s4, s4, 0x3000
	s_addc_u32 s5, s5, 0
	s_add_u32 s6, s6, 0x1000
	s_addc_u32 s7, s7, 0
	global_load_dword v73, v3, s[4:5]
	global_load_dword v81, v4, s[4:5]
	global_load_dword v89, v5, s[4:5]
	global_load_dword v97, v6, s[6:7]
	s_add_u32 s4, s4, 0x3000
	s_addc_u32 s5, s5, 0
	s_add_u32 s6, s6, 0x1000
	s_addc_u32 s7, s7, 0
	global_load_dword v74, v3, s[4:5]
	global_load_dword v82, v4, s[4:5]
	global_load_dword v90, v5, s[4:5]
	global_load_dword v98, v6, s[6:7]
	s_add_u32 s4, s4, 0x3000
	s_addc_u32 s5, s5, 0
	s_add_u32 s6, s6, 0x1000
	s_addc_u32 s7, s7, 0
	global_load_dword v75, v3, s[4:5]
	global_load_dword v83, v4, s[4:5]
	global_load_dword v91, v5, s[4:5]
	global_load_dword v99, v6, s[6:7]
	s_add_u32 s4, s4, 0x3000
	s_addc_u32 s5, s5, 0
	s_add_u32 s6, s6, 0x1000
	s_addc_u32 s7, s7, 0
	global_load_dword v76, v3, s[4:5]
	global_load_dword v84, v4, s[4:5]
	global_load_dword v92, v5, s[4:5]
	global_load_dword v100, v6, s[6:7]
	s_add_u32 s4, s4, 0x3000
	s_addc_u32 s5, s5, 0
	s_add_u32 s6, s6, 0x1000
	s_addc_u32 s7, s7, 0
	global_load_dword v77, v3, s[4:5]
	global_load_dword v85, v4, s[4:5]
	global_load_dword v93, v5, s[4:5]
	global_load_dword v101, v6, s[6:7]
	global_load_dword v102, v7, s[8:9]
	global_load_dword v110, v8, s[10:11]
	s_add_u32 s8, s8, 0x1400
	s_addc_u32 s9, s9, 0
	s_add_u32 s10, s10, 0x1000
	s_addc_u32 s11, s11, 0
	global_load_dword v103, v7, s[8:9]
	global_load_dword v111, v8, s[10:11]
	s_add_u32 s8, s8, 0x1400
	s_addc_u32 s9, s9, 0
	s_add_u32 s10, s10, 0x1000
	s_addc_u32 s11, s11, 0
	global_load_dword v104, v7, s[8:9]
	global_load_dword v112, v8, s[10:11]
	s_add_u32 s8, s8, 0x1400
	s_addc_u32 s9, s9, 0
	s_add_u32 s10, s10, 0x1000
	s_addc_u32 s11, s11, 0
	global_load_dword v105, v7, s[8:9]
	global_load_dword v113, v8, s[10:11]
	s_add_u32 s8, s8, 0x1400
	s_addc_u32 s9, s9, 0
	s_add_u32 s10, s10, 0x1000
	s_addc_u32 s11, s11, 0
	global_load_dword v106, v7, s[8:9]
	global_load_dword v114, v8, s[10:11]
	s_add_u32 s8, s8, 0x1400
	s_addc_u32 s9, s9, 0
	s_add_u32 s10, s10, 0x1000
	s_addc_u32 s11, s11, 0
	global_load_dword v107, v7, s[8:9]
	global_load_dword v115, v8, s[10:11]
	s_add_u32 s8, s8, 0x1400
	s_addc_u32 s9, s9, 0
	s_add_u32 s10, s10, 0x1000
	s_addc_u32 s11, s11, 0
	global_load_dword v108, v7, s[8:9]
	global_load_dword v116, v8, s[10:11]
	s_add_u32 s8, s8, 0x1400
	s_addc_u32 s9, s9, 0
	s_add_u32 s10, s10, 0x1000
	s_addc_u32 s11, s11, 0
	global_load_dword v109, v7, s[8:9]
	global_load_dword v117, v8, s[10:11]
	s_cmp_lt_u32 s96, 64
	s_cbranch_scc0 .Ltr_pathb
;     const size_t total = (size_t)N * (K / 8);
; #pragma unroll 1
;     for (size_t i = (size_t)bid * NTHR + threadIdx.x; i < total; i += (size_t)nb * NTHR) {
;         const int n = (int)(i % N), kc = (int)(i / N);
;         float v[8];
; #pragma unroll
;         for (int j = 0; j < 8; ++j) v[j] = W[(size_t)(kc * 8 + j) * N + n];
;         uint4 r; r.x = pack2(v[0], v[1]); r.y = pack2(v[2], v[3]); r.z = pack2(v[4], v[5]); r.w = pack2(v[6], v[7]);
;         if (FRAG) *(uint4*)&WT[((size_t)((kc >> 1) * (N / 32) + (n >> 5)) * 64 + (n & 31) + 32 * (kc & 1)) * 8] = r;
;         else *(uint4*)&WT[(size_t)n * K + kc * 8] = r;
;     }
;     ...
;     transpose_cvt(P.in[10], 1024, 3072, (bfr*)(P.ws + WS_WINT0), bid, nb);
;     transpose_cvt(P.in[11], 1024, 1024, (bfr*)(P.ws + WS_WOUTT0), bid, nb);
;     transpose_cvt(P.in[22], 1024, 1280, (bfr*)(P.ws + WS_WINT1), bid, nb);
;     transpose_cvt(P.in[23], 1024, 1024, (bfr*)(P.ws + WS_WOUTT1), bid, nb);
;     transpose_cvt<1>(P.in[36], 1024, 256, (bfr*)(P.ws + WS_ROUT), bid, nb);
;     transpose_cvt<1>(P.in[36] + 1024 * 256, 1024, 256, (bfr*)(P.ws + WS_ROUT) + 256 * 1024, bid, nb);
;     transpose_cvt(P.in[34], 512, 512, (bfr*)(P.ws + WS_GLUT), bid, nb);
	s_waitcnt vmcnt(16)
	v_cvt_pk_bf16_f32 v70, v70, v71
	v_cvt_pk_bf16_f32 v71, v72, v73
	v_cvt_pk_bf16_f32 v72, v74, v75
	v_cvt_pk_bf16_f32 v73, v76, v77
	global_store_dwordx4 v12, v[70:73], s[42:43]
	v_cvt_pk_bf16_f32 v78, v78, v79
	v_cvt_pk_bf16_f32 v79, v80, v81
	v_cvt_pk_bf16_f32 v80, v82, v83
	v_cvt_pk_bf16_f32 v81, v84, v85
	global_store_dwordx4 v13, v[78:81], s[42:43]
	v_cvt_pk_bf16_f32 v86, v86, v87
	v_cvt_pk_bf16_f32 v87, v88, v89
	v_cvt_pk_bf16_f32 v88, v90, v91
	v_cvt_pk_bf16_f32 v89, v92, v93
	global_store_dwordx4 v14, v[86:89], s[42:43]
	v_cvt_pk_bf16_f32 v94, v94, v95
	v_cvt_pk_bf16_f32 v95, v96, v97
	v_cvt_pk_bf16_f32 v96, v98, v99
	v_cvt_pk_bf16_f32 v97, v100, v101
	global_store_dwordx4 v15, v[94:97], s[42:43]
	global_load_dword v118, v9, s[18:19]
	global_load_dword v126, v10, s[12:13]
	global_load_dword v134, v10, s[14:15]
	global_load_dword v142, v11, s[16:17]
	s_add_u32 s18, s18, 0x1400
	s_addc_u32 s19, s19, 0
	s_add_u32 s12, s12, 0x400
	s_addc_u32 s13, s13, 0
	s_add_u32 s14, s14, 0x400
	s_addc_u32 s15, s15, 0
	s_add_u32 s16, s16, 0x800
	s_addc_u32 s17, s17, 0
	global_load_dword v119, v9, s[18:19]
	global_load_dword v127, v10, s[12:13]
	global_load_dword v135, v10, s[14:15]
	global_load_dword v143, v11, s[16:17]
	s_add_u32 s18, s18, 0x1400
	s_addc_u32 s19, s19, 0
	s_add_u32 s12, s12, 0x400
	s_addc_u32 s13, s13, 0
	s_add_u32 s14, s14, 0x400
	s_addc_u32 s15, s15, 0
	s_add_u32 s16, s16, 0x800
	s_addc_u32 s17, s17, 0
	global_load_dword v120, v9, s[18:19]
	global_load_dword v128, v10, s[12:13]
	global_load_dword v136, v10, s[14:15]
	global_load_dword v144, v11, s[16:17]
	s_add_u32 s18, s18, 0x1400
	s_addc_u32 s19, s19, 0
	s_add_u32 s12, s12, 0x400
	s_addc_u32 s13, s13, 0
	s_add_u32 s14, s14, 0x400
	s_addc_u32 s15, s15, 0
	s_add_u32 s16, s16, 0x800
	s_addc_u32 s17, s17, 0
	global_load_dword v121, v9, s[18:19]
	global_load_dword v129, v10, s[12:13]
	global_load_dword v137, v10, s[14:15]
	global_load_dword v145, v11, s[16:17]
	s_add_u32 s18, s18, 0x1400
	s_addc_u32 s19, s19, 0
	s_add_u32 s12, s12, 0x400
	s_addc_u32 s13, s13, 0
	s_add_u32 s14, s14, 0x400
	s_addc_u32 s15, s15, 0
	s_add_u32 s16, s16, 0x800
	s_addc_u32 s17, s17, 0
	global_load_dword v122, v9, s[18:19]
	global_load_dword v130, v10, s[12:13]
	global_load_dword v138, v10, s[14:15]
	global_load_dword v146, v11, s[16:17]
	s_add_u32 s18, s18, 0x1400
	s_addc_u32 s19, s19, 0
	s_add_u32 s12, s12, 0x400
	s_addc_u32 s13, s13, 0
	s_add_u32 s14, s14, 0x400
	s_addc_u32 s15, s15, 0
	s_add_u32 s16, s16, 0x800
	s_addc_u32 s17, s17, 0
	global_load_dword v123, v9, s[18:19]
	global_load_dword v131, v10, s[12:13]
	global_load_dword v139, v10, s[14:15]
	global_load_dword v147, v11, s[16:17]
	s_add_u32 s18, s18, 0x1400
	s_addc_u32 s19, s19, 0
	s_add_u32 s12, s12, 0x400
	s_addc_u32 s13, s13, 0
	s_add_u32 s14, s14, 0x400
	s_addc_u32 s15, s15, 0
	s_add_u32 s16, s16, 0x800
	s_addc_u32 s17, s17, 0
	global_load_dword v124, v9, s[18:19]
	global_load_dword v132, v10, s[12:13]
	global_load_dword v140, v10, s[14:15]
	global_load_dword v148, v11, s[16:17]
	s_add_u32 s18, s18, 0x1400
	s_addc_u32 s19, s19, 0
	s_add_u32 s12, s12, 0x400
	s_addc_u32 s13, s13, 0
	s_add_u32 s14, s14, 0x400
	s_addc_u32 s15, s15, 0
	s_add_u32 s16, s16, 0x800
	s_addc_u32 s17, s17, 0
	global_load_dword v125, v9, s[18:19]
	global_load_dword v133, v10, s[12:13]
	global_load_dword v141, v10, s[14:15]
	global_load_dword v149, v11, s[16:17]
	s_waitcnt vmcnt(36)
	v_cvt_pk_bf16_f32 v102, v102, v103
	v_cvt_pk_bf16_f32 v103, v104, v105
	v_cvt_pk_bf16_f32 v104, v106, v107
	v_cvt_pk_bf16_f32 v105, v108, v109
	global_store_dwordx4 v16, v[102:105], s[42:43]
	v_cvt_pk_bf16_f32 v110, v110, v111
	v_cvt_pk_bf16_f32 v111, v112, v113
	v_cvt_pk_bf16_f32 v112, v114, v115
	v_cvt_pk_bf16_f32 v113, v116, v117
	global_store_dwordx4 v17, v[110:113], s[42:43]
	s_waitcnt vmcnt(2)
	v_cvt_pk_bf16_f32 v118, v118, v119
	v_cvt_pk_bf16_f32 v119, v120, v121
	v_cvt_pk_bf16_f32 v120, v122, v123
	v_cvt_pk_bf16_f32 v121, v124, v125
	global_store_dwordx4 v18, v[118:121], s[42:43]
	v_cvt_pk_bf16_f32 v126, v126, v127
	v_cvt_pk_bf16_f32 v127, v128, v129
	v_cvt_pk_bf16_f32 v128, v130, v131
	v_cvt_pk_bf16_f32 v129, v132, v133
	global_store_dwordx4 v19, v[126:129], s[42:43]
	v_cvt_pk_bf16_f32 v134, v134, v135
	v_cvt_pk_bf16_f32 v135, v136, v137
	v_cvt_pk_bf16_f32 v136, v138, v139
	v_cvt_pk_bf16_f32 v137, v140, v141
	global_store_dwordx4 v20, v[134:137], s[42:43]
	v_cvt_pk_bf16_f32 v142, v142, v143
	v_cvt_pk_bf16_f32 v143, v144, v145
	v_cvt_pk_bf16_f32 v144, v146, v147
	v_cvt_pk_bf16_f32 v145, v148, v149
	global_store_dwordx4 v21, v[142:145], s[42:43]
	s_branch .Ltr_done
